# fp8 gate epilogue: clamp on the fma replaces max(rcp,1) (one VALU op fewer per element), on top of v83
# speedup vs baseline: 1.0080x; 1.0002x over previous
.LBB0_178:
	v_lshl_add_u32 v8, s20, 8, v194
	v_ashrrev_i32_e32 v9, 31, v8
	s_nop 15
	s_nop 15
	v_lshl_add_u64 v[10:11], v[8:9], 2, s[4:5]
	global_load_dword v22, v[10:11], off
	v_or_b32_e32 v16, 16, v8
	v_ashrrev_i32_e32 v17, 31, v16
	v_lshl_add_u64 v[6:7], v[16:17], 2, s[4:5]
	global_load_dword v21, v[6:7], off
	v_or_b32_e32 v14, 32, v8
	v_ashrrev_i32_e32 v15, 31, v14
	v_or_b32_e32 v12, 48, v8
	v_lshl_add_u64 v[6:7], v[14:15], 2, s[4:5]
	v_ashrrev_i32_e32 v13, 31, v12
	global_load_dword v20, v[6:7], off
	v_lshl_add_u64 v[6:7], v[12:13], 2, s[4:5]
	v_lshl_or_b32 v4, s21, 8, v211
	global_load_dword v9, v[6:7], off
	global_load_dword v226, v[10:11], off offset:512
	global_load_dword v229, v[10:11], off offset:576
	global_load_dword v240, v[10:11], off offset:640
	global_load_dword v251, v[10:11], off offset:704
	v_mov_b64_e32 v[6:7], s[8:9]
	s_movk_i32 s13, 0x7200
	v_ashrrev_i32_e32 v5, 31, v4
	v_mad_i64_i32 v[18:19], s[20:21], v8, s13, v[6:7]
	v_lshl_add_u64 v[18:19], v[18:19], 0, v[4:5]
	s_andn2_b64 vcc, exec, s[36:37]
	s_waitcnt lgkmcnt(0)
	s_waitcnt vmcnt(7)
	v_mul_f32_e32 v13, 0x3c000000, v22
	v_mul_f32_e32 v13, 0xbfb8aa3b, v13
	v_mul_f32_e32 v15, v160, v13
	v_mul_f32_e32 v17, v156, v13
	v_exp_f32_e32 v15, v15
	v_exp_f32_e32 v17, v17
	v_mul_f32_e32 v22, v161, v13
	v_mul_f32_e32 v23, v157, v13
	v_exp_f32_e32 v22, v22
	v_exp_f32_e32 v23, v23
	v_fma_f32 v15, v15, v227, v227 clamp
	v_fma_f32 v17, v17, v227, v227 clamp
	v_rcp_f32_e32 v15, v15
	v_rcp_f32_e32 v17, v17
	v_fma_f32 v22, v22, v227, v227 clamp
	v_fma_f32 v23, v23, v227, v227 clamp
	v_rcp_f32_e32 v22, v22
	v_rcp_f32_e32 v23, v23
	v_cvt_pk_u8_f32 v15, v15, 0, 0
	v_cvt_pk_u8_f32 v17, v17, 0, 0
	v_cvt_pk_u8_f32 v15, v22, 1, v15
	v_cvt_pk_u8_f32 v17, v23, 1, v17
	v_mul_f32_e32 v22, v162, v13
	v_mul_f32_e32 v23, v158, v13
	v_exp_f32_e32 v22, v22
	v_exp_f32_e32 v23, v23
	s_waitcnt vmcnt(4)
	v_mul_f32_e32 v9, 0x3c000000, v9
	v_mul_f32_e32 v9, 0xbfb8aa3b, v9
	v_fma_f32 v22, v22, v227, v227 clamp
	v_fma_f32 v23, v23, v227, v227 clamp
	v_rcp_f32_e32 v22, v22
	v_rcp_f32_e32 v23, v23
	v_cvt_pk_u8_f32 v15, v22, 2, v15
	v_cvt_pk_u8_f32 v17, v23, 2, v17
	v_mul_f32_e32 v22, v163, v13
	v_mul_f32_e32 v23, v159, v13
	v_exp_f32_e32 v22, v22
	v_exp_f32_e32 v23, v23
	v_fma_f32 v22, v22, v227, v227 clamp
	v_fma_f32 v23, v23, v227, v227 clamp
	v_rcp_f32_e32 v22, v22
	v_rcp_f32_e32 v23, v23
	v_cvt_pk_u8_f32 v22, v22, 3, v15
	v_cvt_pk_u8_f32 v23, v23, 3, v17
	v_mul_f32_e32 v15, v152, v13
	global_store_dwordx2 v[18:19], v[22:23], off
	v_exp_f32_e32 v15, v15
	v_mul_f32_e32 v22, v153, v13
	v_exp_f32_e32 v22, v22
	v_mul_f32_e32 v17, v148, v13
	v_fma_f32 v15, v15, v227, v227 clamp
	v_rcp_f32_e32 v15, v15
	v_fma_f32 v22, v22, v227, v227 clamp
	v_rcp_f32_e32 v22, v22
	v_exp_f32_e32 v17, v17
	v_cvt_pk_u8_f32 v15, v15, 0, 0
	v_mul_f32_e32 v23, v149, v13
	v_exp_f32_e32 v23, v23
	v_cvt_pk_u8_f32 v15, v22, 1, v15
	v_mul_f32_e32 v22, v154, v13
	v_exp_f32_e32 v22, v22
	v_fma_f32 v17, v17, v227, v227 clamp
	v_rcp_f32_e32 v17, v17
	v_fma_f32 v23, v23, v227, v227 clamp
	v_rcp_f32_e32 v23, v23
	v_fma_f32 v22, v22, v227, v227 clamp
	v_rcp_f32_e32 v22, v22
	v_cvt_pk_u8_f32 v17, v17, 0, 0
	v_cvt_pk_u8_f32 v17, v23, 1, v17
	v_mul_f32_e32 v23, v150, v13
	v_exp_f32_e32 v23, v23
	v_cvt_pk_u8_f32 v15, v22, 2, v15
	v_mul_f32_e32 v22, v155, v13
	v_mul_f32_e32 v13, v151, v13
	v_exp_f32_e32 v13, v13
	v_exp_f32_e32 v22, v22
	v_fma_f32 v23, v23, v227, v227 clamp
	v_rcp_f32_e32 v23, v23
	v_fma_f32 v13, v13, v227, v227 clamp
	v_fma_f32 v22, v22, v227, v227 clamp
	v_rcp_f32_e32 v13, v13
	v_rcp_f32_e32 v22, v22
	v_cvt_pk_u8_f32 v17, v23, 2, v17
	v_cvt_pk_u8_f32 v23, v13, 3, v17
	v_mul_f32_e32 v13, 0x3c000000, v21
	v_cvt_pk_u8_f32 v22, v22, 3, v15
	v_mul_f32_e32 v13, 0xbfb8aa3b, v13
	global_store_dwordx2 v[18:19], v[22:23], off offset:128
	v_mul_f32_e32 v15, v144, v13
	v_mul_f32_e32 v18, v140, v13
	v_exp_f32_e32 v15, v15
	v_exp_f32_e32 v18, v18
	v_mul_f32_e32 v19, v145, v13
	v_mul_f32_e32 v21, v141, v13
	v_exp_f32_e32 v19, v19
	v_exp_f32_e32 v21, v21
	v_fma_f32 v15, v15, v227, v227 clamp
	v_fma_f32 v18, v18, v227, v227 clamp
	v_rcp_f32_e32 v15, v15
	v_rcp_f32_e32 v18, v18
	v_fma_f32 v19, v19, v227, v227 clamp
	v_fma_f32 v21, v21, v227, v227 clamp
	v_rcp_f32_e32 v19, v19
	v_rcp_f32_e32 v21, v21
	v_cvt_pk_u8_f32 v15, v15, 0, 0
	v_cvt_pk_u8_f32 v18, v18, 0, 0
	v_cvt_pk_u8_f32 v15, v19, 1, v15
	v_cvt_pk_u8_f32 v18, v21, 1, v18
	v_mul_f32_e32 v19, v146, v13
	v_mul_f32_e32 v21, v142, v13
	v_exp_f32_e32 v19, v19
	v_exp_f32_e32 v21, v21
	v_mad_i64_i32 v[16:17], s[20:21], v16, s13, v[6:7]
	v_fma_f32 v19, v19, v227, v227 clamp
	v_fma_f32 v21, v21, v227, v227 clamp
	v_rcp_f32_e32 v19, v19
	v_rcp_f32_e32 v21, v21
	v_lshl_add_u64 v[16:17], v[16:17], 0, v[4:5]
	v_cvt_pk_u8_f32 v15, v19, 2, v15
	v_cvt_pk_u8_f32 v19, v21, 2, v18
	v_mul_f32_e32 v18, v147, v13
	v_mul_f32_e32 v21, v143, v13
	v_exp_f32_e32 v18, v18
	v_exp_f32_e32 v21, v21
	v_fma_f32 v18, v18, v227, v227 clamp
	v_fma_f32 v21, v21, v227, v227 clamp
	v_rcp_f32_e32 v18, v18
	v_rcp_f32_e32 v21, v21
	v_cvt_pk_u8_f32 v18, v18, 3, v15
	v_cvt_pk_u8_f32 v19, v21, 3, v19
	global_store_dwordx2 v[16:17], v[18:19], off
	v_mul_f32_e32 v15, v136, v13
	v_mul_f32_e32 v18, v132, v13
	v_exp_f32_e32 v15, v15
	v_exp_f32_e32 v18, v18
	v_mul_f32_e32 v19, v137, v13
	v_mul_f32_e32 v21, v133, v13
	v_exp_f32_e32 v19, v19
	v_exp_f32_e32 v21, v21
	v_fma_f32 v15, v15, v227, v227 clamp
	v_fma_f32 v18, v18, v227, v227 clamp
	v_rcp_f32_e32 v15, v15
	v_rcp_f32_e32 v18, v18
	v_fma_f32 v19, v19, v227, v227 clamp
	v_fma_f32 v21, v21, v227, v227 clamp
	v_rcp_f32_e32 v19, v19
	v_rcp_f32_e32 v21, v21
	v_cvt_pk_u8_f32 v15, v15, 0, 0
	v_cvt_pk_u8_f32 v18, v18, 0, 0
	v_cvt_pk_u8_f32 v15, v19, 1, v15
	v_cvt_pk_u8_f32 v18, v21, 1, v18
	v_mul_f32_e32 v19, v138, v13
	v_mul_f32_e32 v21, v134, v13
	v_exp_f32_e32 v19, v19
	v_exp_f32_e32 v21, v21
	v_fma_f32 v19, v19, v227, v227 clamp
	v_fma_f32 v21, v21, v227, v227 clamp
	v_rcp_f32_e32 v19, v19
	v_rcp_f32_e32 v21, v21
	v_cvt_pk_u8_f32 v15, v19, 2, v15
	v_cvt_pk_u8_f32 v19, v21, 2, v18
	v_mul_f32_e32 v18, v139, v13
	v_mul_f32_e32 v13, v135, v13
	v_exp_f32_e32 v13, v13
	v_exp_f32_e32 v18, v18
	v_fma_f32 v13, v13, v227, v227 clamp
	v_fma_f32 v18, v18, v227, v227 clamp
	v_rcp_f32_e32 v13, v13
	v_rcp_f32_e32 v18, v18
	v_cvt_pk_u8_f32 v19, v13, 3, v19
	v_mul_f32_e32 v13, 0x3c000000, v20
	v_cvt_pk_u8_f32 v18, v18, 3, v15
	v_mul_f32_e32 v13, 0xbfb8aa3b, v13
	global_store_dwordx2 v[16:17], v[18:19], off offset:128
	v_mul_f32_e32 v16, v128, v13
	v_mul_f32_e32 v17, v124, v13
	v_exp_f32_e32 v16, v16
	v_exp_f32_e32 v17, v17
	v_mul_f32_e32 v18, v129, v13
	v_mul_f32_e32 v19, v125, v13
	v_exp_f32_e32 v18, v18
	v_exp_f32_e32 v19, v19
	v_fma_f32 v16, v16, v227, v227 clamp
	v_fma_f32 v17, v17, v227, v227 clamp
	v_rcp_f32_e32 v16, v16
	v_rcp_f32_e32 v17, v17
	v_fma_f32 v18, v18, v227, v227 clamp
	v_fma_f32 v19, v19, v227, v227 clamp
	v_rcp_f32_e32 v18, v18
	v_rcp_f32_e32 v19, v19
	v_cvt_pk_u8_f32 v16, v16, 0, 0
	v_cvt_pk_u8_f32 v17, v17, 0, 0
	v_cvt_pk_u8_f32 v16, v18, 1, v16
	v_cvt_pk_u8_f32 v17, v19, 1, v17
	v_mul_f32_e32 v18, v130, v13
	v_mul_f32_e32 v19, v126, v13
	v_exp_f32_e32 v18, v18
	v_exp_f32_e32 v19, v19
	v_mad_i64_i32 v[14:15], s[20:21], v14, s13, v[6:7]
	v_fma_f32 v18, v18, v227, v227 clamp
	v_fma_f32 v19, v19, v227, v227 clamp
	v_rcp_f32_e32 v18, v18
	v_rcp_f32_e32 v19, v19
	v_lshl_add_u64 v[14:15], v[14:15], 0, v[4:5]
	v_cvt_pk_u8_f32 v16, v18, 2, v16
	v_cvt_pk_u8_f32 v17, v19, 2, v17
	v_mul_f32_e32 v18, v131, v13
	v_mul_f32_e32 v19, v127, v13
	v_exp_f32_e32 v18, v18
	v_exp_f32_e32 v19, v19
	v_fma_f32 v18, v18, v227, v227 clamp
	v_fma_f32 v19, v19, v227, v227 clamp
	v_rcp_f32_e32 v18, v18
	v_rcp_f32_e32 v19, v19
	v_cvt_pk_u8_f32 v16, v18, 3, v16
	v_cvt_pk_u8_f32 v17, v19, 3, v17
	global_store_dwordx2 v[14:15], v[16:17], off
	v_mul_f32_e32 v16, v120, v13
	v_exp_f32_e32 v16, v16
	v_mul_f32_e32 v18, v121, v13
	v_exp_f32_e32 v18, v18
	v_mul_f32_e32 v17, v116, v13
	v_fma_f32 v16, v16, v227, v227 clamp
	v_rcp_f32_e32 v16, v16
	v_fma_f32 v18, v18, v227, v227 clamp
	v_rcp_f32_e32 v18, v18
	v_exp_f32_e32 v17, v17
	v_cvt_pk_u8_f32 v16, v16, 0, 0
	v_mul_f32_e32 v19, v117, v13
	v_exp_f32_e32 v19, v19
	v_cvt_pk_u8_f32 v16, v18, 1, v16
	v_mul_f32_e32 v18, v122, v13
	v_exp_f32_e32 v18, v18
	v_fma_f32 v17, v17, v227, v227 clamp
	v_rcp_f32_e32 v17, v17
	v_fma_f32 v19, v19, v227, v227 clamp
	v_rcp_f32_e32 v19, v19
	v_fma_f32 v18, v18, v227, v227 clamp
	v_rcp_f32_e32 v18, v18
	v_cvt_pk_u8_f32 v17, v17, 0, 0
	v_cvt_pk_u8_f32 v17, v19, 1, v17
	v_mul_f32_e32 v19, v118, v13
	v_exp_f32_e32 v19, v19
	v_cvt_pk_u8_f32 v16, v18, 2, v16
	v_mul_f32_e32 v18, v123, v13
	v_mul_f32_e32 v13, v119, v13
	v_exp_f32_e32 v18, v18
	v_exp_f32_e32 v13, v13
	v_fma_f32 v19, v19, v227, v227 clamp
	v_rcp_f32_e32 v19, v19
	v_fma_f32 v18, v18, v227, v227 clamp
	v_fma_f32 v13, v13, v227, v227 clamp
	v_rcp_f32_e32 v18, v18
	v_rcp_f32_e32 v13, v13
	v_cvt_pk_u8_f32 v17, v19, 2, v17
	v_cvt_pk_u8_f32 v16, v18, 3, v16
	v_cvt_pk_u8_f32 v17, v13, 3, v17
	global_store_dwordx2 v[14:15], v[16:17], off offset:128
	v_mul_f32_e32 v14, v112, v9
	v_mul_f32_e32 v15, v108, v9
	v_exp_f32_e32 v14, v14
	v_exp_f32_e32 v15, v15
	v_mul_f32_e32 v16, v113, v9
	v_mul_f32_e32 v17, v109, v9
	v_exp_f32_e32 v16, v16
	v_exp_f32_e32 v17, v17
	v_fma_f32 v14, v14, v227, v227 clamp
	v_fma_f32 v15, v15, v227, v227 clamp
	v_rcp_f32_e32 v14, v14
	v_rcp_f32_e32 v15, v15
	v_fma_f32 v16, v16, v227, v227 clamp
	v_fma_f32 v17, v17, v227, v227 clamp
	v_rcp_f32_e32 v16, v16
	v_rcp_f32_e32 v17, v17
	v_cvt_pk_u8_f32 v14, v14, 0, 0
	v_cvt_pk_u8_f32 v15, v15, 0, 0
	v_cvt_pk_u8_f32 v14, v16, 1, v14
	v_cvt_pk_u8_f32 v15, v17, 1, v15
	v_mul_f32_e32 v16, v114, v9
	v_mul_f32_e32 v17, v110, v9
	v_exp_f32_e32 v16, v16
	v_exp_f32_e32 v17, v17
	v_mad_i64_i32 v[12:13], s[20:21], v12, s13, v[6:7]
	v_fma_f32 v16, v16, v227, v227 clamp
	v_fma_f32 v17, v17, v227, v227 clamp
	v_rcp_f32_e32 v16, v16
	v_rcp_f32_e32 v17, v17
	v_lshl_add_u64 v[12:13], v[12:13], 0, v[4:5]
	v_add_u32_e32 v18, 0x90, v8
	v_cvt_pk_u8_f32 v14, v16, 2, v14
	v_cvt_pk_u8_f32 v15, v17, 2, v15
	v_mul_f32_e32 v16, v115, v9
	v_mul_f32_e32 v17, v111, v9
	v_exp_f32_e32 v16, v16
	v_exp_f32_e32 v17, v17
	v_fma_f32 v16, v16, v227, v227 clamp
	v_fma_f32 v17, v17, v227, v227 clamp
	v_rcp_f32_e32 v16, v16
	v_rcp_f32_e32 v17, v17
	v_cvt_pk_u8_f32 v14, v16, 3, v14
	v_cvt_pk_u8_f32 v15, v17, 3, v15
	global_store_dwordx2 v[12:13], v[14:15], off
	v_mul_f32_e32 v14, v104, v9
	v_exp_f32_e32 v14, v14
	v_mul_f32_e32 v16, v105, v9
	v_exp_f32_e32 v16, v16
	v_mul_f32_e32 v15, v100, v9
	v_fma_f32 v14, v14, v227, v227 clamp
	v_rcp_f32_e32 v14, v14
	v_fma_f32 v16, v16, v227, v227 clamp
	v_rcp_f32_e32 v16, v16
	v_exp_f32_e32 v15, v15
	v_cvt_pk_u8_f32 v14, v14, 0, 0
	v_mul_f32_e32 v17, v101, v9
	v_exp_f32_e32 v17, v17
	v_cvt_pk_u8_f32 v14, v16, 1, v14
	v_mul_f32_e32 v16, v106, v9
	v_exp_f32_e32 v16, v16
	v_fma_f32 v15, v15, v227, v227 clamp
	v_rcp_f32_e32 v15, v15
	v_fma_f32 v17, v17, v227, v227 clamp
	v_rcp_f32_e32 v17, v17
	v_fma_f32 v16, v16, v227, v227 clamp
	v_rcp_f32_e32 v16, v16
	v_cvt_pk_u8_f32 v15, v15, 0, 0
	v_cvt_pk_u8_f32 v15, v17, 1, v15
	v_mul_f32_e32 v17, v102, v9
	v_exp_f32_e32 v17, v17
	v_cvt_pk_u8_f32 v14, v16, 2, v14
	v_mul_f32_e32 v16, v107, v9
	v_mul_f32_e32 v9, v103, v9
	v_exp_f32_e32 v16, v16
	v_exp_f32_e32 v9, v9
	v_fma_f32 v17, v17, v227, v227 clamp
	v_rcp_f32_e32 v17, v17
	v_fma_f32 v16, v16, v227, v227 clamp
	v_fma_f32 v9, v9, v227, v227 clamp
	v_rcp_f32_e32 v16, v16
	v_rcp_f32_e32 v9, v9
	v_cvt_pk_u8_f32 v15, v17, 2, v15
	v_cvt_pk_u8_f32 v14, v16, 3, v14
	v_cvt_pk_u8_f32 v15, v9, 3, v15
	global_store_dwordx2 v[12:13], v[14:15], off offset:128
	s_nop 1
	s_waitcnt vmcnt(11)
	v_mov_b32_e32 v15, v226
	v_add_u32_e32 v9, 0x80, v8
	s_waitcnt vmcnt(10)
	v_mov_b32_e32 v19, v229
	s_waitcnt vmcnt(9)
	v_mov_b32_e32 v13, v240
	v_add_u32_e32 v14, 0xa0, v8
	s_waitcnt vmcnt(8)
	v_mov_b32_e32 v10, v251
	v_add_u32_e32 v12, 0xb0, v8
	v_mad_i64_i32 v[8:9], s[20:21], v9, s13, v[6:7]
	v_lshl_add_u64 v[8:9], v[8:9], 0, v[4:5]
	s_waitcnt lgkmcnt(0)
	v_mul_f32_e32 v11, 0x3c000000, v15
	v_mul_f32_e32 v11, 0xbfb8aa3b, v11
	v_mul_f32_e32 v15, v96, v11
	v_mul_f32_e32 v16, v92, v11
	v_exp_f32_e32 v15, v15
	v_exp_f32_e32 v16, v16
	v_mul_f32_e32 v17, v97, v11
	v_mul_f32_e32 v20, v93, v11
	v_exp_f32_e32 v17, v17
	v_exp_f32_e32 v20, v20
	v_fma_f32 v15, v15, v227, v227 clamp
	v_fma_f32 v16, v16, v227, v227 clamp
	v_rcp_f32_e32 v15, v15
	v_rcp_f32_e32 v16, v16
	v_fma_f32 v17, v17, v227, v227 clamp
	v_fma_f32 v20, v20, v227, v227 clamp
	v_rcp_f32_e32 v17, v17
	v_rcp_f32_e32 v20, v20
	v_cvt_pk_u8_f32 v15, v15, 0, 0
	v_cvt_pk_u8_f32 v16, v16, 0, 0
	v_cvt_pk_u8_f32 v15, v17, 1, v15
	v_cvt_pk_u8_f32 v16, v20, 1, v16
	v_mul_f32_e32 v17, v98, v11
	v_mul_f32_e32 v20, v94, v11
	v_exp_f32_e32 v17, v17
	v_exp_f32_e32 v20, v20
	v_fma_f32 v17, v17, v227, v227 clamp
	v_fma_f32 v20, v20, v227, v227 clamp
	v_rcp_f32_e32 v17, v17
	v_rcp_f32_e32 v20, v20
	v_cvt_pk_u8_f32 v15, v17, 2, v15
	v_cvt_pk_u8_f32 v17, v20, 2, v16
	v_mul_f32_e32 v16, v99, v11
	v_mul_f32_e32 v20, v95, v11
	v_exp_f32_e32 v16, v16
	v_exp_f32_e32 v20, v20
	v_fma_f32 v16, v16, v227, v227 clamp
	v_fma_f32 v20, v20, v227, v227 clamp
	v_rcp_f32_e32 v16, v16
	v_rcp_f32_e32 v20, v20
	v_cvt_pk_u8_f32 v16, v16, 3, v15
	v_cvt_pk_u8_f32 v17, v20, 3, v17
	global_store_dwordx2 v[8:9], v[16:17], off
	v_mul_f32_e32 v15, v88, v11
	v_mul_f32_e32 v16, v84, v11
	v_exp_f32_e32 v15, v15
	v_exp_f32_e32 v16, v16
	v_mul_f32_e32 v17, v89, v11
	v_mul_f32_e32 v20, v85, v11
	v_exp_f32_e32 v17, v17
	v_exp_f32_e32 v20, v20
	v_fma_f32 v15, v15, v227, v227 clamp
	v_fma_f32 v16, v16, v227, v227 clamp
	v_rcp_f32_e32 v15, v15
	v_rcp_f32_e32 v16, v16
	v_fma_f32 v17, v17, v227, v227 clamp
	v_fma_f32 v20, v20, v227, v227 clamp
	v_rcp_f32_e32 v17, v17
	v_rcp_f32_e32 v20, v20
	v_cvt_pk_u8_f32 v15, v15, 0, 0
	v_cvt_pk_u8_f32 v16, v16, 0, 0
	v_cvt_pk_u8_f32 v15, v17, 1, v15
	v_cvt_pk_u8_f32 v16, v20, 1, v16
	v_mul_f32_e32 v17, v90, v11
	v_mul_f32_e32 v20, v86, v11
	v_exp_f32_e32 v17, v17
	v_exp_f32_e32 v20, v20
	v_fma_f32 v17, v17, v227, v227 clamp
	v_fma_f32 v20, v20, v227, v227 clamp
	v_rcp_f32_e32 v17, v17
	v_rcp_f32_e32 v20, v20
	v_cvt_pk_u8_f32 v15, v17, 2, v15
	v_cvt_pk_u8_f32 v17, v20, 2, v16
	v_mul_f32_e32 v16, v91, v11
	v_mul_f32_e32 v11, v87, v11
	v_exp_f32_e32 v11, v11
	v_exp_f32_e32 v16, v16
	v_fma_f32 v11, v11, v227, v227 clamp
	v_fma_f32 v16, v16, v227, v227 clamp
	v_rcp_f32_e32 v11, v11
	v_rcp_f32_e32 v16, v16
	v_cvt_pk_u8_f32 v17, v11, 3, v17
	v_mul_f32_e32 v11, 0x3c000000, v19
	v_cvt_pk_u8_f32 v16, v16, 3, v15
	v_mul_f32_e32 v11, 0xbfb8aa3b, v11
	global_store_dwordx2 v[8:9], v[16:17], off offset:128
	v_mul_f32_e32 v15, v80, v11
	v_mul_f32_e32 v16, v76, v11
	v_mad_i64_i32 v[8:9], s[20:21], v18, s13, v[6:7]
	v_exp_f32_e32 v15, v15
	v_exp_f32_e32 v16, v16
	v_mul_f32_e32 v17, v81, v11
	v_mul_f32_e32 v18, v77, v11
	v_exp_f32_e32 v17, v17
	v_exp_f32_e32 v18, v18
	v_fma_f32 v15, v15, v227, v227 clamp
	v_fma_f32 v16, v16, v227, v227 clamp
	v_rcp_f32_e32 v15, v15
	v_rcp_f32_e32 v16, v16
	v_fma_f32 v17, v17, v227, v227 clamp
	v_fma_f32 v18, v18, v227, v227 clamp
	v_rcp_f32_e32 v17, v17
	v_rcp_f32_e32 v18, v18
	v_cvt_pk_u8_f32 v15, v15, 0, 0
	v_cvt_pk_u8_f32 v16, v16, 0, 0
	v_cvt_pk_u8_f32 v15, v17, 1, v15
	v_cvt_pk_u8_f32 v16, v18, 1, v16
	v_mul_f32_e32 v17, v82, v11
	v_mul_f32_e32 v18, v78, v11
	v_exp_f32_e32 v17, v17
	v_exp_f32_e32 v18, v18
	v_lshl_add_u64 v[8:9], v[8:9], 0, v[4:5]
	v_fma_f32 v17, v17, v227, v227 clamp
	v_fma_f32 v18, v18, v227, v227 clamp
	v_rcp_f32_e32 v17, v17
	v_rcp_f32_e32 v18, v18
	v_cvt_pk_u8_f32 v15, v17, 2, v15
	v_cvt_pk_u8_f32 v17, v18, 2, v16
	v_mul_f32_e32 v16, v83, v11
	v_mul_f32_e32 v18, v79, v11
	v_exp_f32_e32 v16, v16
	v_exp_f32_e32 v18, v18
	v_fma_f32 v16, v16, v227, v227 clamp
	v_fma_f32 v18, v18, v227, v227 clamp
	v_rcp_f32_e32 v16, v16
	v_rcp_f32_e32 v18, v18
	v_cvt_pk_u8_f32 v16, v16, 3, v15
	v_cvt_pk_u8_f32 v17, v18, 3, v17
	global_store_dwordx2 v[8:9], v[16:17], off
	v_mul_f32_e32 v15, v72, v11
	v_mul_f32_e32 v16, v68, v11
	v_exp_f32_e32 v15, v15
	v_exp_f32_e32 v16, v16
	v_mul_f32_e32 v17, v73, v11
	v_mul_f32_e32 v18, v69, v11
	v_exp_f32_e32 v17, v17
	v_exp_f32_e32 v18, v18
	v_fma_f32 v15, v15, v227, v227 clamp
	v_fma_f32 v16, v16, v227, v227 clamp
	v_rcp_f32_e32 v15, v15
	v_rcp_f32_e32 v16, v16
	v_fma_f32 v17, v17, v227, v227 clamp
	v_fma_f32 v18, v18, v227, v227 clamp
	v_rcp_f32_e32 v17, v17
	v_rcp_f32_e32 v18, v18
	v_cvt_pk_u8_f32 v15, v15, 0, 0
	v_cvt_pk_u8_f32 v16, v16, 0, 0
	v_cvt_pk_u8_f32 v15, v17, 1, v15
	v_cvt_pk_u8_f32 v16, v18, 1, v16
	v_mul_f32_e32 v17, v74, v11
	v_mul_f32_e32 v18, v70, v11
	v_exp_f32_e32 v17, v17
	v_exp_f32_e32 v18, v18
	v_fma_f32 v17, v17, v227, v227 clamp
	v_fma_f32 v18, v18, v227, v227 clamp
	v_rcp_f32_e32 v17, v17
	v_rcp_f32_e32 v18, v18
	v_cvt_pk_u8_f32 v15, v17, 2, v15
	v_cvt_pk_u8_f32 v17, v18, 2, v16
	v_mul_f32_e32 v16, v75, v11
	v_mul_f32_e32 v11, v71, v11
	v_exp_f32_e32 v11, v11
	v_exp_f32_e32 v16, v16
	v_fma_f32 v11, v11, v227, v227 clamp
	v_fma_f32 v16, v16, v227, v227 clamp
	v_rcp_f32_e32 v11, v11
	v_rcp_f32_e32 v16, v16
	v_cvt_pk_u8_f32 v17, v11, 3, v17
	v_mul_f32_e32 v11, 0x3c000000, v13
	v_cvt_pk_u8_f32 v16, v16, 3, v15
	v_mul_f32_e32 v11, 0xbfb8aa3b, v11
	global_store_dwordx2 v[8:9], v[16:17], off offset:128
	v_mad_i64_i32 v[8:9], s[20:21], v14, s13, v[6:7]
	v_mul_f32_e32 v13, v64, v11
	v_mul_f32_e32 v14, v60, v11
	v_exp_f32_e32 v13, v13
	v_exp_f32_e32 v14, v14
	v_mul_f32_e32 v15, v65, v11
	v_mul_f32_e32 v16, v61, v11
	v_exp_f32_e32 v15, v15
	v_exp_f32_e32 v16, v16
	v_fma_f32 v13, v13, v227, v227 clamp
	v_fma_f32 v14, v14, v227, v227 clamp
	v_rcp_f32_e32 v13, v13
	v_rcp_f32_e32 v14, v14
	v_fma_f32 v15, v15, v227, v227 clamp
	v_fma_f32 v16, v16, v227, v227 clamp
	v_rcp_f32_e32 v15, v15
	v_rcp_f32_e32 v16, v16
	v_cvt_pk_u8_f32 v13, v13, 0, 0
	v_cvt_pk_u8_f32 v14, v14, 0, 0
	v_cvt_pk_u8_f32 v13, v15, 1, v13
	v_cvt_pk_u8_f32 v14, v16, 1, v14
	v_mul_f32_e32 v15, v66, v11
	v_mul_f32_e32 v16, v62, v11
	v_exp_f32_e32 v15, v15
	v_exp_f32_e32 v16, v16
	v_lshl_add_u64 v[8:9], v[8:9], 0, v[4:5]
	v_mad_i64_i32 v[6:7], s[20:21], v12, s13, v[6:7]
	v_fma_f32 v15, v15, v227, v227 clamp
	v_fma_f32 v16, v16, v227, v227 clamp
	v_rcp_f32_e32 v15, v15
	v_rcp_f32_e32 v16, v16
	v_lshl_add_u64 v[4:5], v[6:7], 0, v[4:5]
	v_mul_f32_e32 v6, 0x3c000000, v10
	v_cvt_pk_u8_f32 v13, v15, 2, v13
	v_cvt_pk_u8_f32 v15, v16, 2, v14
	v_mul_f32_e32 v14, v67, v11
	v_mul_f32_e32 v16, v63, v11
	v_exp_f32_e32 v14, v14
	v_exp_f32_e32 v16, v16
	s_mov_b64 s[20:21], -1
	v_fma_f32 v14, v14, v227, v227 clamp
	v_fma_f32 v16, v16, v227, v227 clamp
	v_rcp_f32_e32 v14, v14
	v_rcp_f32_e32 v16, v16
	v_cvt_pk_u8_f32 v14, v14, 3, v13
	v_cvt_pk_u8_f32 v15, v16, 3, v15
	global_store_dwordx2 v[8:9], v[14:15], off
	v_mul_f32_e32 v13, v56, v11
	v_mul_f32_e32 v14, v52, v11
	v_exp_f32_e32 v13, v13
	v_exp_f32_e32 v14, v14
	v_mul_f32_e32 v15, v57, v11
	v_mul_f32_e32 v16, v53, v11
	v_exp_f32_e32 v15, v15
	v_exp_f32_e32 v16, v16
	v_fma_f32 v13, v13, v227, v227 clamp
	v_fma_f32 v14, v14, v227, v227 clamp
	v_rcp_f32_e32 v13, v13
	v_rcp_f32_e32 v14, v14
	v_fma_f32 v15, v15, v227, v227 clamp
	v_fma_f32 v16, v16, v227, v227 clamp
	v_rcp_f32_e32 v15, v15
	v_rcp_f32_e32 v16, v16
	v_cvt_pk_u8_f32 v13, v13, 0, 0
	v_cvt_pk_u8_f32 v14, v14, 0, 0
	v_cvt_pk_u8_f32 v13, v15, 1, v13
	v_cvt_pk_u8_f32 v14, v16, 1, v14
	v_mul_f32_e32 v15, v58, v11
	v_mul_f32_e32 v16, v54, v11
	v_exp_f32_e32 v15, v15
	v_exp_f32_e32 v16, v16
	v_fma_f32 v15, v15, v227, v227 clamp
	v_fma_f32 v16, v16, v227, v227 clamp
	v_rcp_f32_e32 v15, v15
	v_rcp_f32_e32 v16, v16
	v_cvt_pk_u8_f32 v13, v15, 2, v13
	v_cvt_pk_u8_f32 v15, v16, 2, v14
	v_mul_f32_e32 v14, v59, v11
	v_mul_f32_e32 v11, v55, v11
	v_exp_f32_e32 v14, v14
	v_exp_f32_e32 v11, v11
	v_fma_f32 v14, v14, v227, v227 clamp
	v_fma_f32 v11, v11, v227, v227 clamp
	v_rcp_f32_e32 v14, v14
	v_rcp_f32_e32 v11, v11
	v_cvt_pk_u8_f32 v14, v14, 3, v13
	v_cvt_pk_u8_f32 v15, v11, 3, v15
	global_store_dwordx2 v[8:9], v[14:15], off offset:128
	v_mul_f32_e32 v8, 0xbfb8aa3b, v6
	v_mul_f32_e32 v6, v48, v8
	v_mul_f32_e32 v7, v44, v8
	v_exp_f32_e32 v6, v6
	v_exp_f32_e32 v7, v7
	v_mul_f32_e32 v9, v49, v8
	v_mul_f32_e32 v10, v45, v8
	v_exp_f32_e32 v9, v9
	v_exp_f32_e32 v10, v10
	v_fma_f32 v6, v6, v227, v227 clamp
	v_fma_f32 v7, v7, v227, v227 clamp
	v_rcp_f32_e32 v6, v6
	v_rcp_f32_e32 v7, v7
	v_fma_f32 v9, v9, v227, v227 clamp
	v_fma_f32 v10, v10, v227, v227 clamp
	v_rcp_f32_e32 v9, v9
	v_rcp_f32_e32 v10, v10
	v_cvt_pk_u8_f32 v6, v6, 0, 0
	v_cvt_pk_u8_f32 v7, v7, 0, 0
	v_cvt_pk_u8_f32 v6, v9, 1, v6
	v_cvt_pk_u8_f32 v7, v10, 1, v7
	v_mul_f32_e32 v9, v50, v8
	v_mul_f32_e32 v10, v46, v8
	v_exp_f32_e32 v9, v9
	v_exp_f32_e32 v10, v10
	v_fma_f32 v9, v9, v227, v227 clamp
	v_fma_f32 v10, v10, v227, v227 clamp
	v_rcp_f32_e32 v9, v9
	v_rcp_f32_e32 v10, v10
	v_cvt_pk_u8_f32 v6, v9, 2, v6
	v_cvt_pk_u8_f32 v7, v10, 2, v7
	v_mul_f32_e32 v9, v51, v8
	v_mul_f32_e32 v10, v47, v8
	v_exp_f32_e32 v9, v9
	v_exp_f32_e32 v10, v10
	v_fma_f32 v9, v9, v227, v227 clamp
	v_fma_f32 v10, v10, v227, v227 clamp
	v_rcp_f32_e32 v9, v9
	v_rcp_f32_e32 v10, v10
	v_cvt_pk_u8_f32 v6, v9, 3, v6
	v_cvt_pk_u8_f32 v7, v10, 3, v7
	global_store_dwordx2 v[4:5], v[6:7], off
	v_mul_f32_e32 v6, v40, v8
	v_exp_f32_e32 v6, v6
	v_mul_f32_e32 v9, v41, v8
	v_exp_f32_e32 v9, v9
	v_mul_f32_e32 v7, v36, v8
	v_fma_f32 v6, v6, v227, v227 clamp
	v_rcp_f32_e32 v6, v6
	v_fma_f32 v9, v9, v227, v227 clamp
	v_rcp_f32_e32 v9, v9
	v_exp_f32_e32 v7, v7
	v_cvt_pk_u8_f32 v6, v6, 0, 0
	v_mul_f32_e32 v10, v37, v8
	v_exp_f32_e32 v10, v10
	v_cvt_pk_u8_f32 v6, v9, 1, v6
	v_mul_f32_e32 v9, v42, v8
	v_exp_f32_e32 v9, v9
	v_fma_f32 v7, v7, v227, v227 clamp
	v_rcp_f32_e32 v7, v7
	v_fma_f32 v10, v10, v227, v227 clamp
	v_rcp_f32_e32 v10, v10
	v_fma_f32 v9, v9, v227, v227 clamp
	v_rcp_f32_e32 v9, v9
	v_cvt_pk_u8_f32 v7, v7, 0, 0
	v_cvt_pk_u8_f32 v7, v10, 1, v7
	v_mul_f32_e32 v10, v38, v8
	v_exp_f32_e32 v10, v10
	v_cvt_pk_u8_f32 v6, v9, 2, v6
	v_mul_f32_e32 v9, v43, v8
	v_mul_f32_e32 v8, v39, v8
	v_exp_f32_e32 v9, v9
	v_exp_f32_e32 v8, v8
	v_fma_f32 v10, v10, v227, v227 clamp
	v_rcp_f32_e32 v10, v10
	v_fma_f32 v9, v9, v227, v227 clamp
	v_fma_f32 v8, v8, v227, v227 clamp
	v_rcp_f32_e32 v9, v9
	v_rcp_f32_e32 v8, v8
	v_cvt_pk_u8_f32 v7, v10, 2, v7
	v_cvt_pk_u8_f32 v6, v9, 3, v6
	v_cvt_pk_u8_f32 v7, v8, 3, v7
	global_store_dwordx2 v[4:5], v[6:7], off offset:128
	s_cbranch_vccnz .LBB0_167
	s_andn2_b64 vcc, exec, s[0:1]
	s_cbranch_vccnz .LBB0_166
	s_barrier
	s_branch .LBB0_166
